# P9+P10: first K-iteration of every unit peeled (first MFMA per accumulator takes C=0, no zeroing v_movs) and its first two DMA waits no longer wait for the previous unit's epilogue store acks (vmcnt 1
# speedup vs baseline: 1.0076x; 1.0076x over previous
.LBB0_1353:
	s_lshl_b64 s[6:7], s[26:27], 16
	s_lshl_b32 s27, s26, 2
	s_add_i32 s27, s27, 0
	s_add_i32 s27, s27, 0x21040
	s_add_u32 s42, s25, s6
	v_mov_b32_e32 v169, v163
	v_mov_b32_e32 v173, v163
	s_addc_u32 s43, s56, s7
	s_mov_b32 s29, -2
	s_mov_b64 s[44:45], s[2:3]
	s_branch .LBB0_1356
.Lp9_peel:
	v_add_u32_e32 v2, s85, v185
	v_add_u32_e32 v14, s86, v185
	ds_read_b128 v[18:21], v2
	ds_read_b128 v[22:25], v2 offset:1024
	ds_read_b128 v[26:29], v2 offset:2048
	ds_read_b128 v[30:33], v2 offset:3072
	ds_read_b128 v[2:5], v14
	ds_read_b128 v[6:9], v14 offset:1024
	ds_read_b128 v[10:13], v14 offset:2048
	ds_read_b128 v[14:17], v14 offset:3072
	v_lshl_add_u64 v[222:223], s[50:51], 0, v[168:169]
	s_add_i32 m0, s59, 0xc000
	ds_read_b128 v[174:177], v188
	ds_read_b128 v[178:181], v188 offset:1024
	ds_read_b128 v[198:201], v188 offset:2048
	ds_read_b128 v[202:205], v188 offset:3072
	ds_read_b128 v[206:209], v188 offset:4096
	ds_read_b128 v[210:213], v188 offset:5120
	ds_read_b128 v[214:217], v188 offset:6144
	ds_read_b128 v[218:221], v188 offset:7168
	global_load_lds_dwordx4 v[222:223], off
	v_lshl_add_u64 v[222:223], s[50:51], 0, v[172:173]
	s_add_i32 m0, s59, 0xe000
	s_nop 0
	global_load_lds_dwordx4 v[222:223], off
	s_cmp_lt_u32 s63, 2
	s_cbranch_scc0 .Lp9_pw1
	s_waitcnt vmcnt(8)
.Lp9_pw1:
	s_waitcnt vmcnt(16)
	s_waitcnt lgkmcnt(0)
	s_barrier
	s_setprio 1
	s_waitcnt lgkmcnt(0)
	v_mfma_f32_16x16x128_f8f6f4 v[158:161], v[18:25], v[174:181], 0
	v_mfma_f32_16x16x128_f8f6f4 v[154:157], v[26:33], v[174:181], 0
	v_mfma_f32_16x16x128_f8f6f4 v[142:145], v[18:25], v[198:205], 0
	v_mfma_f32_16x16x128_f8f6f4 v[134:137], v[26:33], v[198:205], 0
	v_mfma_f32_16x16x128_f8f6f4 v[126:129], v[18:25], v[206:213], 0
	v_mfma_f32_16x16x128_f8f6f4 v[118:121], v[26:33], v[206:213], 0
	v_mfma_f32_16x16x128_f8f6f4 v[110:113], v[18:25], v[214:221], 0
	v_mfma_f32_16x16x128_f8f6f4 v[102:105], v[26:33], v[214:221], 0
	s_setprio 0
	s_setprio 1
	v_mfma_f32_16x16x128_f8f6f4 v[150:153], v[2:9], v[174:181], 0
	v_mfma_f32_16x16x128_f8f6f4 v[146:149], v[10:17], v[174:181], 0
	v_mfma_f32_16x16x128_f8f6f4 v[138:141], v[2:9], v[198:205], 0
	v_mfma_f32_16x16x128_f8f6f4 v[130:133], v[10:17], v[198:205], 0
	v_mfma_f32_16x16x128_f8f6f4 v[122:125], v[2:9], v[206:213], 0
	v_mfma_f32_16x16x128_f8f6f4 v[114:117], v[10:17], v[206:213], 0
	v_mfma_f32_16x16x128_f8f6f4 v[106:109], v[2:9], v[214:221], 0
	v_mfma_f32_16x16x128_f8f6f4 v[98:101], v[10:17], v[214:221], 0
	s_setprio 0
	s_barrier
	s_add_i32 s37, s85, s58
	v_lshl_add_u64 v[174:175], s[46:47], 0, v[164:165]
	s_mov_b32 m0, s37
	ds_read_b128 v[198:201], v188 offset:16384
	ds_read_b128 v[202:205], v188 offset:17408
	ds_read_b128 v[206:209], v188 offset:18432
	ds_read_b128 v[210:213], v188 offset:19456
	ds_read_b128 v[214:217], v188 offset:20480
	ds_read_b128 v[218:221], v188 offset:21504
	ds_read_b128 v[222:225], v188 offset:22528
	ds_read_b128 v[226:229], v188 offset:23552
	global_load_lds_dwordx4 v[174:175], off
	s_add_i32 m0, s37, 0x2000
	s_add_u32 s50, s46, 0x40000
	v_lshl_add_u64 v[176:177], s[46:47], 0, v[166:167]
	s_addc_u32 s51, s47, 0
	s_add_i32 s37, s86, s58
	global_load_lds_dwordx4 v[176:177], off
	v_lshl_add_u64 v[178:179], s[50:51], 0, v[164:165]
	s_mov_b32 m0, s37
	v_cndmask_b32_e64 v162, v196, v192, s[6:7]
	global_load_lds_dwordx4 v[178:179], off
	v_lshl_add_u64 v[178:179], s[50:51], 0, v[166:167]
	s_add_i32 m0, s37, 0x2000
	s_nop 0
	global_load_lds_dwordx4 v[178:179], off
	s_mov_b32 m0, s59
	v_lshl_add_u64 v[178:179], s[48:49], 0, v[162:163]
	global_load_lds_dwordx4 v162, s[48:49]
	v_cndmask_b32_e64 v162, v170, v191, s[6:7]
	s_mov_b32 m0, s60
	v_lshl_add_u64 v[180:181], s[48:49], 0, v[162:163]
	global_load_lds_dwordx4 v162, s[48:49]
	s_cmp_lt_u32 s63, 2
	s_cbranch_scc0 .Lp9_pw2
	s_waitcnt vmcnt(8)
.Lp9_pw2:
	s_waitcnt vmcnt(16)
	s_waitcnt lgkmcnt(0)
	s_barrier
	s_setprio 1
	s_waitcnt lgkmcnt(0)
	v_mfma_f32_16x16x128_f8f6f4 v[94:97], v[18:25], v[198:205], 0
	v_mfma_f32_16x16x128_f8f6f4 v[86:89], v[26:33], v[198:205], 0
	v_mfma_f32_16x16x128_f8f6f4 v[78:81], v[18:25], v[206:213], 0
	v_mfma_f32_16x16x128_f8f6f4 v[70:73], v[26:33], v[206:213], 0
	v_mfma_f32_16x16x128_f8f6f4 v[62:65], v[18:25], v[214:221], 0
	v_mfma_f32_16x16x128_f8f6f4 v[54:57], v[26:33], v[214:221], 0
	v_mfma_f32_16x16x128_f8f6f4 v[46:49], v[18:25], v[222:229], 0
	v_mfma_f32_16x16x128_f8f6f4 v[38:41], v[26:33], v[222:229], 0
	s_setprio 0
	s_setprio 1
	v_mfma_f32_16x16x128_f8f6f4 v[90:93], v[2:9], v[198:205], 0
	v_mfma_f32_16x16x128_f8f6f4 v[82:85], v[10:17], v[198:205], 0
	v_mfma_f32_16x16x128_f8f6f4 v[74:77], v[2:9], v[206:213], 0
	v_mfma_f32_16x16x128_f8f6f4 v[66:69], v[10:17], v[206:213], 0
	v_mfma_f32_16x16x128_f8f6f4 v[58:61], v[2:9], v[214:221], 0
	v_mfma_f32_16x16x128_f8f6f4 v[50:53], v[10:17], v[214:221], 0
	v_mfma_f32_16x16x128_f8f6f4 v[42:45], v[2:9], v[222:229], 0
	v_mfma_f32_16x16x128_f8f6f4 v[34:37], v[10:17], v[222:229], 0
	s_setprio 0
	s_barrier
	s_add_i32 s37, 0, 0x18000
	s_add_i32 s50, 0, 0x1c000
	v_add_u32_e32 v14, s37, v185
	v_add_u32_e32 v30, s50, v185
	ds_read_b128 v[2:5], v14
	ds_read_b128 v[6:9], v14 offset:1024
	ds_read_b128 v[10:13], v14 offset:2048
	ds_read_b128 v[14:17], v14 offset:3072
	ds_read_b128 v[18:21], v30
	ds_read_b128 v[22:25], v30 offset:1024
	ds_read_b128 v[26:29], v30 offset:2048
	ds_read_b128 v[30:33], v30 offset:3072
	s_mov_b32 m0, s61
	v_cndmask_b32_e64 v162, v168, v190, s[6:7]
	ds_read_b128 v[198:201], v188 offset:32768
	ds_read_b128 v[202:205], v188 offset:33792
	ds_read_b128 v[206:209], v188 offset:34816
	ds_read_b128 v[210:213], v188 offset:35840
	ds_read_b128 v[214:217], v188 offset:36864
	ds_read_b128 v[218:221], v188 offset:37888
	ds_read_b128 v[222:225], v188 offset:38912
	ds_read_b128 v[226:229], v188 offset:39936
	global_load_lds_dwordx4 v162, s[48:49]
	v_cndmask_b32_e64 v162, v172, v193, s[6:7]
	s_mov_b32 m0, s62
	s_nop 0
	global_load_lds_dwordx4 v162, s[48:49]
	s_waitcnt vmcnt(8)
	s_waitcnt lgkmcnt(0)
	s_barrier
	s_setprio 1
	s_waitcnt lgkmcnt(0)
	v_mfma_f32_16x16x128_f8f6f4 v[158:161], v[2:9], v[198:205], v[158:161]
	v_mfma_f32_16x16x128_f8f6f4 v[154:157], v[10:17], v[198:205], v[154:157]
	v_mfma_f32_16x16x128_f8f6f4 v[142:145], v[2:9], v[206:213], v[142:145]
	v_mfma_f32_16x16x128_f8f6f4 v[134:137], v[10:17], v[206:213], v[134:137]
	v_mfma_f32_16x16x128_f8f6f4 v[126:129], v[2:9], v[214:221], v[126:129]
	v_mfma_f32_16x16x128_f8f6f4 v[118:121], v[10:17], v[214:221], v[118:121]
	v_mfma_f32_16x16x128_f8f6f4 v[110:113], v[2:9], v[222:229], v[110:113]
	v_mfma_f32_16x16x128_f8f6f4 v[102:105], v[10:17], v[222:229], v[102:105]
	s_setprio 0
	s_setprio 1
	v_mfma_f32_16x16x128_f8f6f4 v[150:153], v[18:25], v[198:205], v[150:153]
	v_mfma_f32_16x16x128_f8f6f4 v[146:149], v[26:33], v[198:205], v[146:149]
	v_mfma_f32_16x16x128_f8f6f4 v[138:141], v[18:25], v[206:213], v[138:141]
	v_mfma_f32_16x16x128_f8f6f4 v[130:133], v[26:33], v[206:213], v[130:133]
	v_mfma_f32_16x16x128_f8f6f4 v[122:125], v[18:25], v[214:221], v[122:125]
	v_mfma_f32_16x16x128_f8f6f4 v[114:117], v[26:33], v[214:221], v[114:117]
	v_mfma_f32_16x16x128_f8f6f4 v[106:109], v[18:25], v[222:229], v[106:109]
	v_mfma_f32_16x16x128_f8f6f4 v[98:101], v[26:33], v[222:229], v[98:101]
	s_setprio 0
	s_barrier
	s_add_i32 s6, s37, s58
	v_lshl_add_u64 v[174:175], v[174:175], 0, s[16:17]
	s_mov_b32 m0, s6
	ds_read_b128 v[198:201], v188 offset:49152
	ds_read_b128 v[202:205], v188 offset:50176
	ds_read_b128 v[206:209], v188 offset:51200
	ds_read_b128 v[210:213], v188 offset:52224
	ds_read_b128 v[214:217], v188 offset:53248
	ds_read_b128 v[218:221], v188 offset:54272
	ds_read_b128 v[222:225], v188 offset:55296
	ds_read_b128 v[226:229], v188 offset:56320
	global_load_lds_dwordx4 v[174:175], off
	s_add_i32 m0, s6, 0x2000
	s_add_u32 s6, s46, 0x40080
	v_lshl_add_u64 v[174:175], v[176:177], 0, s[16:17]
	s_addc_u32 s7, s47, 0
	s_add_i32 s37, s50, s58
	global_load_lds_dwordx4 v[174:175], off
	v_lshl_add_u64 v[174:175], s[6:7], 0, v[164:165]
	s_mov_b32 m0, s37
	s_nop 0
	global_load_lds_dwordx4 v[174:175], off
	v_lshl_add_u64 v[174:175], s[6:7], 0, v[166:167]
	s_add_i32 m0, s37, 0x2000
	s_nop 0
	global_load_lds_dwordx4 v[174:175], off
	v_lshl_add_u64 v[174:175], v[178:179], 0, s[16:17]
	s_mov_b32 m0, s66
	s_nop 0
	global_load_lds_dwordx4 v[174:175], off
	v_lshl_add_u64 v[174:175], v[180:181], 0, s[16:17]
	s_mov_b32 m0, s67
	s_nop 0
	global_load_lds_dwordx4 v[174:175], off
	s_waitcnt vmcnt(8)
	s_waitcnt lgkmcnt(0)
	s_barrier
	s_setprio 1
	s_waitcnt lgkmcnt(0)
	v_mfma_f32_16x16x128_f8f6f4 v[94:97], v[2:9], v[198:205], v[94:97]
	v_mfma_f32_16x16x128_f8f6f4 v[86:89], v[10:17], v[198:205], v[86:89]
	v_mfma_f32_16x16x128_f8f6f4 v[78:81], v[2:9], v[206:213], v[78:81]
	v_mfma_f32_16x16x128_f8f6f4 v[70:73], v[10:17], v[206:213], v[70:73]
	v_mfma_f32_16x16x128_f8f6f4 v[62:65], v[2:9], v[214:221], v[62:65]
	v_mfma_f32_16x16x128_f8f6f4 v[54:57], v[10:17], v[214:221], v[54:57]
	v_mfma_f32_16x16x128_f8f6f4 v[46:49], v[2:9], v[222:229], v[46:49]
	v_mfma_f32_16x16x128_f8f6f4 v[38:41], v[10:17], v[222:229], v[38:41]
	s_setprio 0
	s_setprio 1
	v_mfma_f32_16x16x128_f8f6f4 v[90:93], v[18:25], v[198:205], v[90:93]
	v_mfma_f32_16x16x128_f8f6f4 v[82:85], v[26:33], v[198:205], v[82:85]
	v_mfma_f32_16x16x128_f8f6f4 v[74:77], v[18:25], v[206:213], v[74:77]
	v_mfma_f32_16x16x128_f8f6f4 v[66:69], v[26:33], v[206:213], v[66:69]
	v_mfma_f32_16x16x128_f8f6f4 v[58:61], v[18:25], v[214:221], v[58:61]
	v_mfma_f32_16x16x128_f8f6f4 v[50:53], v[26:33], v[214:221], v[50:53]
	v_mfma_f32_16x16x128_f8f6f4 v[42:45], v[18:25], v[222:229], v[42:45]
	v_mfma_f32_16x16x128_f8f6f4 v[34:37], v[26:33], v[222:229], v[34:37]
	s_setprio 0
	s_barrier
	s_add_i32 s29, s29, 2
	s_add_u32 s44, s44, 0x100
	s_addc_u32 s45, s45, 0
	s_add_u32 s38, s38, 0x100
	s_addc_u32 s39, s39, 0
	s_cmp_gt_u32 s29, 13
	s_cbranch_scc1 .LBB0_1368
	s_branch .LBB0_1356
.LBB0_1355:
	s_cmp_eq_u32 s29, -2
	s_cbranch_scc1 .Lp9_peel
	v_add_u32_e32 v2, s85, v185
	v_add_u32_e32 v14, s86, v185
	ds_read_b128 v[18:21], v2
	ds_read_b128 v[22:25], v2 offset:1024
	ds_read_b128 v[26:29], v2 offset:2048
	ds_read_b128 v[30:33], v2 offset:3072
	ds_read_b128 v[2:5], v14
	ds_read_b128 v[6:9], v14 offset:1024
	ds_read_b128 v[10:13], v14 offset:2048
	ds_read_b128 v[14:17], v14 offset:3072
	v_lshl_add_u64 v[222:223], s[50:51], 0, v[168:169]
	s_add_i32 m0, s59, 0xc000
	ds_read_b128 v[174:177], v188
	ds_read_b128 v[178:181], v188 offset:1024
	ds_read_b128 v[198:201], v188 offset:2048
	ds_read_b128 v[202:205], v188 offset:3072
	ds_read_b128 v[206:209], v188 offset:4096
	ds_read_b128 v[210:213], v188 offset:5120
	ds_read_b128 v[214:217], v188 offset:6144
	ds_read_b128 v[218:221], v188 offset:7168
	global_load_lds_dwordx4 v[222:223], off
	v_lshl_add_u64 v[222:223], s[50:51], 0, v[172:173]
	s_add_i32 m0, s59, 0xe000
	s_nop 0
	global_load_lds_dwordx4 v[222:223], off
	s_waitcnt vmcnt(8)
	s_waitcnt lgkmcnt(0)
	s_barrier
	s_setprio 1
	s_waitcnt lgkmcnt(0)
	v_mfma_f32_16x16x128_f8f6f4 v[158:161], v[18:25], v[174:181], v[158:161]
	v_mfma_f32_16x16x128_f8f6f4 v[154:157], v[26:33], v[174:181], v[154:157]
	v_mfma_f32_16x16x128_f8f6f4 v[142:145], v[18:25], v[198:205], v[142:145]
	v_mfma_f32_16x16x128_f8f6f4 v[134:137], v[26:33], v[198:205], v[134:137]
	v_mfma_f32_16x16x128_f8f6f4 v[126:129], v[18:25], v[206:213], v[126:129]
	v_mfma_f32_16x16x128_f8f6f4 v[118:121], v[26:33], v[206:213], v[118:121]
	v_mfma_f32_16x16x128_f8f6f4 v[110:113], v[18:25], v[214:221], v[110:113]
	v_mfma_f32_16x16x128_f8f6f4 v[102:105], v[26:33], v[214:221], v[102:105]
	s_setprio 0
	s_setprio 1
	v_mfma_f32_16x16x128_f8f6f4 v[150:153], v[2:9], v[174:181], v[150:153]
	v_mfma_f32_16x16x128_f8f6f4 v[146:149], v[10:17], v[174:181], v[146:149]
	v_mfma_f32_16x16x128_f8f6f4 v[138:141], v[2:9], v[198:205], v[138:141]
	v_mfma_f32_16x16x128_f8f6f4 v[130:133], v[10:17], v[198:205], v[130:133]
	v_mfma_f32_16x16x128_f8f6f4 v[122:125], v[2:9], v[206:213], v[122:125]
	v_mfma_f32_16x16x128_f8f6f4 v[114:117], v[10:17], v[206:213], v[114:117]
	v_mfma_f32_16x16x128_f8f6f4 v[106:109], v[2:9], v[214:221], v[106:109]
	v_mfma_f32_16x16x128_f8f6f4 v[98:101], v[10:17], v[214:221], v[98:101]
	s_setprio 0
	s_barrier
	s_add_i32 s37, s85, s58
	v_lshl_add_u64 v[174:175], s[46:47], 0, v[164:165]
	s_mov_b32 m0, s37
	ds_read_b128 v[198:201], v188 offset:16384
	ds_read_b128 v[202:205], v188 offset:17408
	ds_read_b128 v[206:209], v188 offset:18432
	ds_read_b128 v[210:213], v188 offset:19456
	ds_read_b128 v[214:217], v188 offset:20480
	ds_read_b128 v[218:221], v188 offset:21504
	ds_read_b128 v[222:225], v188 offset:22528
	ds_read_b128 v[226:229], v188 offset:23552
	global_load_lds_dwordx4 v[174:175], off
	s_add_i32 m0, s37, 0x2000
	s_add_u32 s50, s46, 0x40000
	v_lshl_add_u64 v[176:177], s[46:47], 0, v[166:167]
	s_addc_u32 s51, s47, 0
	s_add_i32 s37, s86, s58
	global_load_lds_dwordx4 v[176:177], off
	v_lshl_add_u64 v[178:179], s[50:51], 0, v[164:165]
	s_mov_b32 m0, s37
	v_cndmask_b32_e64 v162, v196, v192, s[6:7]
	global_load_lds_dwordx4 v[178:179], off
	v_lshl_add_u64 v[178:179], s[50:51], 0, v[166:167]
	s_add_i32 m0, s37, 0x2000
	s_nop 0
	global_load_lds_dwordx4 v[178:179], off
	s_mov_b32 m0, s59
	v_lshl_add_u64 v[178:179], s[48:49], 0, v[162:163]
	global_load_lds_dwordx4 v162, s[48:49]
	v_cndmask_b32_e64 v162, v170, v191, s[6:7]
	s_mov_b32 m0, s60
	v_lshl_add_u64 v[180:181], s[48:49], 0, v[162:163]
	global_load_lds_dwordx4 v162, s[48:49]
	s_waitcnt vmcnt(8)
	s_waitcnt lgkmcnt(0)
	s_barrier
	s_setprio 1
	s_waitcnt lgkmcnt(0)
	v_mfma_f32_16x16x128_f8f6f4 v[94:97], v[18:25], v[198:205], v[94:97]
	v_mfma_f32_16x16x128_f8f6f4 v[86:89], v[26:33], v[198:205], v[86:89]
	v_mfma_f32_16x16x128_f8f6f4 v[78:81], v[18:25], v[206:213], v[78:81]
	v_mfma_f32_16x16x128_f8f6f4 v[70:73], v[26:33], v[206:213], v[70:73]
	v_mfma_f32_16x16x128_f8f6f4 v[62:65], v[18:25], v[214:221], v[62:65]
	v_mfma_f32_16x16x128_f8f6f4 v[54:57], v[26:33], v[214:221], v[54:57]
	v_mfma_f32_16x16x128_f8f6f4 v[46:49], v[18:25], v[222:229], v[46:49]
	v_mfma_f32_16x16x128_f8f6f4 v[38:41], v[26:33], v[222:229], v[38:41]
	s_setprio 0
	s_setprio 1
	v_mfma_f32_16x16x128_f8f6f4 v[90:93], v[2:9], v[198:205], v[90:93]
	v_mfma_f32_16x16x128_f8f6f4 v[82:85], v[10:17], v[198:205], v[82:85]
	v_mfma_f32_16x16x128_f8f6f4 v[74:77], v[2:9], v[206:213], v[74:77]
	v_mfma_f32_16x16x128_f8f6f4 v[66:69], v[10:17], v[206:213], v[66:69]
	v_mfma_f32_16x16x128_f8f6f4 v[58:61], v[2:9], v[214:221], v[58:61]
	v_mfma_f32_16x16x128_f8f6f4 v[50:53], v[10:17], v[214:221], v[50:53]
	v_mfma_f32_16x16x128_f8f6f4 v[42:45], v[2:9], v[222:229], v[42:45]
	v_mfma_f32_16x16x128_f8f6f4 v[34:37], v[10:17], v[222:229], v[34:37]
	s_setprio 0
	s_barrier
	s_add_i32 s37, 0, 0x18000
	s_add_i32 s50, 0, 0x1c000
	v_add_u32_e32 v14, s37, v185
	v_add_u32_e32 v30, s50, v185
	ds_read_b128 v[2:5], v14
	ds_read_b128 v[6:9], v14 offset:1024
	ds_read_b128 v[10:13], v14 offset:2048
	ds_read_b128 v[14:17], v14 offset:3072
	ds_read_b128 v[18:21], v30
	ds_read_b128 v[22:25], v30 offset:1024
	ds_read_b128 v[26:29], v30 offset:2048
	ds_read_b128 v[30:33], v30 offset:3072
	s_mov_b32 m0, s61
	v_cndmask_b32_e64 v162, v168, v190, s[6:7]
	ds_read_b128 v[198:201], v188 offset:32768
	ds_read_b128 v[202:205], v188 offset:33792
	ds_read_b128 v[206:209], v188 offset:34816
	ds_read_b128 v[210:213], v188 offset:35840
	ds_read_b128 v[214:217], v188 offset:36864
	ds_read_b128 v[218:221], v188 offset:37888
	ds_read_b128 v[222:225], v188 offset:38912
	ds_read_b128 v[226:229], v188 offset:39936
	global_load_lds_dwordx4 v162, s[48:49]
	v_cndmask_b32_e64 v162, v172, v193, s[6:7]
	s_mov_b32 m0, s62
	s_nop 0
	global_load_lds_dwordx4 v162, s[48:49]
	s_waitcnt vmcnt(8)
	s_waitcnt lgkmcnt(0)
	s_barrier
	s_setprio 1
	s_waitcnt lgkmcnt(0)
	v_mfma_f32_16x16x128_f8f6f4 v[158:161], v[2:9], v[198:205], v[158:161]
	v_mfma_f32_16x16x128_f8f6f4 v[154:157], v[10:17], v[198:205], v[154:157]
	v_mfma_f32_16x16x128_f8f6f4 v[142:145], v[2:9], v[206:213], v[142:145]
	v_mfma_f32_16x16x128_f8f6f4 v[134:137], v[10:17], v[206:213], v[134:137]
	v_mfma_f32_16x16x128_f8f6f4 v[126:129], v[2:9], v[214:221], v[126:129]
	v_mfma_f32_16x16x128_f8f6f4 v[118:121], v[10:17], v[214:221], v[118:121]
	v_mfma_f32_16x16x128_f8f6f4 v[110:113], v[2:9], v[222:229], v[110:113]
	v_mfma_f32_16x16x128_f8f6f4 v[102:105], v[10:17], v[222:229], v[102:105]
	s_setprio 0
	s_setprio 1
	v_mfma_f32_16x16x128_f8f6f4 v[150:153], v[18:25], v[198:205], v[150:153]
	v_mfma_f32_16x16x128_f8f6f4 v[146:149], v[26:33], v[198:205], v[146:149]
	v_mfma_f32_16x16x128_f8f6f4 v[138:141], v[18:25], v[206:213], v[138:141]
	v_mfma_f32_16x16x128_f8f6f4 v[130:133], v[26:33], v[206:213], v[130:133]
	v_mfma_f32_16x16x128_f8f6f4 v[122:125], v[18:25], v[214:221], v[122:125]
	v_mfma_f32_16x16x128_f8f6f4 v[114:117], v[26:33], v[214:221], v[114:117]
	v_mfma_f32_16x16x128_f8f6f4 v[106:109], v[18:25], v[222:229], v[106:109]
	v_mfma_f32_16x16x128_f8f6f4 v[98:101], v[26:33], v[222:229], v[98:101]
	s_setprio 0
	s_barrier
	s_add_i32 s6, s37, s58
	v_lshl_add_u64 v[174:175], v[174:175], 0, s[16:17]
	s_mov_b32 m0, s6
	ds_read_b128 v[198:201], v188 offset:49152
	ds_read_b128 v[202:205], v188 offset:50176
	ds_read_b128 v[206:209], v188 offset:51200
	ds_read_b128 v[210:213], v188 offset:52224
	ds_read_b128 v[214:217], v188 offset:53248
	ds_read_b128 v[218:221], v188 offset:54272
	ds_read_b128 v[222:225], v188 offset:55296
	ds_read_b128 v[226:229], v188 offset:56320
	global_load_lds_dwordx4 v[174:175], off
	s_add_i32 m0, s6, 0x2000
	s_add_u32 s6, s46, 0x40080
	v_lshl_add_u64 v[174:175], v[176:177], 0, s[16:17]
	s_addc_u32 s7, s47, 0
	s_add_i32 s37, s50, s58
	global_load_lds_dwordx4 v[174:175], off
	v_lshl_add_u64 v[174:175], s[6:7], 0, v[164:165]
	s_mov_b32 m0, s37
	s_nop 0
	global_load_lds_dwordx4 v[174:175], off
	v_lshl_add_u64 v[174:175], s[6:7], 0, v[166:167]
	s_add_i32 m0, s37, 0x2000
	s_nop 0
	global_load_lds_dwordx4 v[174:175], off
	v_lshl_add_u64 v[174:175], v[178:179], 0, s[16:17]
	s_mov_b32 m0, s66
	s_nop 0
	global_load_lds_dwordx4 v[174:175], off
	v_lshl_add_u64 v[174:175], v[180:181], 0, s[16:17]
	s_mov_b32 m0, s67
	s_nop 0
	global_load_lds_dwordx4 v[174:175], off
	s_waitcnt vmcnt(8)
	s_waitcnt lgkmcnt(0)
	s_barrier
	s_setprio 1
	s_waitcnt lgkmcnt(0)
	v_mfma_f32_16x16x128_f8f6f4 v[94:97], v[2:9], v[198:205], v[94:97]
	v_mfma_f32_16x16x128_f8f6f4 v[86:89], v[10:17], v[198:205], v[86:89]
	v_mfma_f32_16x16x128_f8f6f4 v[78:81], v[2:9], v[206:213], v[78:81]
	v_mfma_f32_16x16x128_f8f6f4 v[70:73], v[10:17], v[206:213], v[70:73]
	v_mfma_f32_16x16x128_f8f6f4 v[62:65], v[2:9], v[214:221], v[62:65]
	v_mfma_f32_16x16x128_f8f6f4 v[54:57], v[10:17], v[214:221], v[54:57]
	v_mfma_f32_16x16x128_f8f6f4 v[46:49], v[2:9], v[222:229], v[46:49]
	v_mfma_f32_16x16x128_f8f6f4 v[38:41], v[10:17], v[222:229], v[38:41]
	s_setprio 0
	s_setprio 1
	v_mfma_f32_16x16x128_f8f6f4 v[90:93], v[18:25], v[198:205], v[90:93]
	v_mfma_f32_16x16x128_f8f6f4 v[82:85], v[26:33], v[198:205], v[82:85]
	v_mfma_f32_16x16x128_f8f6f4 v[74:77], v[18:25], v[206:213], v[74:77]
	v_mfma_f32_16x16x128_f8f6f4 v[66:69], v[26:33], v[206:213], v[66:69]
	v_mfma_f32_16x16x128_f8f6f4 v[58:61], v[18:25], v[214:221], v[58:61]
	v_mfma_f32_16x16x128_f8f6f4 v[50:53], v[26:33], v[214:221], v[50:53]
	v_mfma_f32_16x16x128_f8f6f4 v[42:45], v[18:25], v[222:229], v[42:45]
	v_mfma_f32_16x16x128_f8f6f4 v[34:37], v[26:33], v[222:229], v[34:37]
	s_setprio 0
	s_barrier
	s_add_i32 s29, s29, 2
	s_add_u32 s44, s44, 0x100
	s_addc_u32 s45, s45, 0
	s_add_u32 s38, s38, 0x100
	s_addc_u32 s39, s39, 0
	s_cmp_gt_u32 s29, 13
	s_cbranch_scc1 .LBB0_1368

.LBB0_1439:
	s_ashr_i32 s37, s36, 31
	s_lshl_b64 s[38:39], s[36:37], 19
	s_add_u32 s38, s31, s38
	s_addc_u32 s39, s52, s39
	s_add_u32 s35, s42, 0x100
	s_addc_u32 s11, s43, 0
	s_and_b64 s[46:47], s[6:7], exec
	s_cselect_b32 s11, s39, s11
	s_cselect_b32 s35, s38, s35
	s_mov_b32 s37, -2
	ds_read_b128 v[18:21], v185
	ds_read_b128 v[22:25], v185 offset:1024
	ds_read_b128 v[26:29], v185 offset:2048
	ds_read_b128 v[30:33], v185 offset:3072
	ds_read_b128 v[2:5], v186
	ds_read_b128 v[6:9], v186 offset:1024
	ds_read_b128 v[10:13], v186 offset:2048
	ds_read_b128 v[14:17], v186 offset:3072
	s_add_u32 s50, s42, 0x80
	s_addc_u32 s51, s43, 0
	s_add_u32 s42, s42, 0x100
	s_addc_u32 s43, s43, 0
	s_add_u32 s44, s44, 0x100
	s_addc_u32 s45, s45, 0
	s_cmp_eq_u32 s37, 12
	s_cselect_b32 s48, s35, s42
	s_cselect_b32 s49, s11, s43
	s_cselect_b32 s46, s8, s44
	s_cselect_b32 s47, s9, s45
	v_lshl_add_u64 v[212:213], s[50:51], 0, v[170:171]
	s_add_i32 m0, s1, 0xc000
	ds_read_b128 v[174:177], v187
	ds_read_b128 v[178:181], v187 offset:1024
	ds_read_b128 v[188:191], v187 offset:2048
	ds_read_b128 v[192:195], v187 offset:3072
	ds_read_b128 v[196:199], v187 offset:4096
	ds_read_b128 v[200:203], v187 offset:5120
	ds_read_b128 v[204:207], v187 offset:6144
	ds_read_b128 v[208:211], v187 offset:7168
	global_load_lds_dwordx4 v[212:213], off
	v_lshl_add_u64 v[212:213], s[50:51], 0, v[172:173]
	s_add_i32 m0, s1, 0xe000
	s_nop 0
	global_load_lds_dwordx4 v[212:213], off
	s_cmp_lt_u32 s62, 2
	s_cbranch_scc0 .Lp10_pw1
	s_waitcnt vmcnt(8)
.Lp10_pw1:
	s_waitcnt vmcnt(24)
	s_waitcnt lgkmcnt(0)
	s_barrier
	s_setprio 1
	s_waitcnt lgkmcnt(0)
	v_mfma_f32_16x16x128_f8f6f4 v[158:161], v[18:25], v[174:181], 0
	v_mfma_f32_16x16x128_f8f6f4 v[154:157], v[26:33], v[174:181], 0
	v_mfma_f32_16x16x128_f8f6f4 v[150:153], v[18:25], v[188:195], 0
	v_mfma_f32_16x16x128_f8f6f4 v[146:149], v[26:33], v[188:195], 0
	v_mfma_f32_16x16x128_f8f6f4 v[142:145], v[18:25], v[196:203], 0
	v_mfma_f32_16x16x128_f8f6f4 v[134:137], v[26:33], v[196:203], 0
	v_mfma_f32_16x16x128_f8f6f4 v[118:121], v[18:25], v[204:211], 0
	v_mfma_f32_16x16x128_f8f6f4 v[110:113], v[26:33], v[204:211], 0
	s_setprio 0
	s_setprio 1
	v_mfma_f32_16x16x128_f8f6f4 v[138:141], v[2:9], v[174:181], 0
	v_mfma_f32_16x16x128_f8f6f4 v[130:133], v[10:17], v[174:181], 0
	v_mfma_f32_16x16x128_f8f6f4 v[126:129], v[2:9], v[188:195], 0
	v_mfma_f32_16x16x128_f8f6f4 v[122:125], v[10:17], v[188:195], 0
	v_mfma_f32_16x16x128_f8f6f4 v[114:117], v[2:9], v[196:203], 0
	v_mfma_f32_16x16x128_f8f6f4 v[106:109], v[10:17], v[196:203], 0
	v_mfma_f32_16x16x128_f8f6f4 v[102:105], v[2:9], v[204:211], 0
	v_mfma_f32_16x16x128_f8f6f4 v[98:101], v[10:17], v[204:211], 0
	s_setprio 0
	s_barrier
	s_add_i32 s41, s80, s56
	v_lshl_add_u64 v[174:175], s[46:47], 0, v[164:165]
	s_mov_b32 m0, s41
	ds_read_b128 v[188:191], v187 offset:16384
	ds_read_b128 v[192:195], v187 offset:17408
	ds_read_b128 v[196:199], v187 offset:18432
	ds_read_b128 v[200:203], v187 offset:19456
	ds_read_b128 v[204:207], v187 offset:20480
	ds_read_b128 v[208:211], v187 offset:21504
	ds_read_b128 v[212:215], v187 offset:22528
	ds_read_b128 v[216:219], v187 offset:23552
	global_load_lds_dwordx4 v[174:175], off
	s_add_i32 m0, s41, 0x2000
	s_add_u32 s50, s46, 0x40000
	v_lshl_add_u64 v[176:177], s[46:47], 0, v[162:163]
	s_addc_u32 s51, s47, 0
	s_add_i32 s41, s81, s56
	global_load_lds_dwordx4 v[176:177], off
	v_lshl_add_u64 v[178:179], s[50:51], 0, v[164:165]
	s_mov_b32 m0, s41
	v_lshl_add_u64 v[180:181], s[48:49], 0, v[168:169]
	global_load_lds_dwordx4 v[178:179], off
	v_lshl_add_u64 v[178:179], s[50:51], 0, v[162:163]
	s_add_i32 m0, s41, 0x2000
	s_nop 0
	global_load_lds_dwordx4 v[178:179], off
	v_lshl_add_u64 v[178:179], s[48:49], 0, v[166:167]
	s_mov_b32 m0, s1
	s_nop 0
	global_load_lds_dwordx4 v[178:179], off
	s_mov_b32 m0, s33
	s_nop 0
	global_load_lds_dwordx4 v[180:181], off
	s_cmp_lt_u32 s62, 2
	s_cbranch_scc0 .Lp10_pw2
	s_waitcnt vmcnt(8)
.Lp10_pw2:
	s_waitcnt vmcnt(24)
	s_waitcnt lgkmcnt(0)
	s_barrier
	s_setprio 1
	s_waitcnt lgkmcnt(0)
	v_mfma_f32_16x16x128_f8f6f4 v[94:97], v[18:25], v[188:195], 0
	v_mfma_f32_16x16x128_f8f6f4 v[90:93], v[26:33], v[188:195], 0
	v_mfma_f32_16x16x128_f8f6f4 v[78:81], v[18:25], v[196:203], 0
	v_mfma_f32_16x16x128_f8f6f4 v[66:69], v[26:33], v[196:203], 0
	v_mfma_f32_16x16x128_f8f6f4 v[50:53], v[18:25], v[204:211], 0
	v_mfma_f32_16x16x128_f8f6f4 v[46:49], v[26:33], v[204:211], 0
	v_mfma_f32_16x16x128_f8f6f4 v[38:41], v[18:25], v[212:219], 0
	v_mfma_f32_16x16x128_f8f6f4 v[34:37], v[26:33], v[212:219], 0
	s_setprio 0
	s_setprio 1
	v_mfma_f32_16x16x128_f8f6f4 v[82:85], v[2:9], v[188:195], 0
	v_mfma_f32_16x16x128_f8f6f4 v[70:73], v[10:17], v[188:195], 0
	v_mfma_f32_16x16x128_f8f6f4 v[54:57], v[2:9], v[196:203], 0
	v_mfma_f32_16x16x128_f8f6f4 v[42:45], v[10:17], v[196:203], 0
	v_mfma_f32_16x16x128_f8f6f4 v[74:77], v[2:9], v[204:211], 0
	v_mfma_f32_16x16x128_f8f6f4 v[86:89], v[10:17], v[204:211], 0
	v_mfma_f32_16x16x128_f8f6f4 v[58:61], v[2:9], v[212:219], 0
	v_mfma_f32_16x16x128_f8f6f4 v[62:65], v[10:17], v[212:219], 0
	s_setprio 0
	s_barrier
	s_add_i32 s41, 0, 0x18000
	s_add_i32 s50, 0, 0x1c000
	v_add_u32_e32 v14, s41, v182
	v_add_u32_e32 v30, s50, v182
	ds_read_b128 v[2:5], v14
	ds_read_b128 v[6:9], v14 offset:1024
	ds_read_b128 v[10:13], v14 offset:2048
	ds_read_b128 v[14:17], v14 offset:3072
	ds_read_b128 v[18:21], v30
	ds_read_b128 v[22:25], v30 offset:1024
	ds_read_b128 v[26:29], v30 offset:2048
	ds_read_b128 v[30:33], v30 offset:3072
	s_mov_b32 m0, s54
	v_lshl_add_u64 v[220:221], s[48:49], 0, v[170:171]
	ds_read_b128 v[188:191], v187 offset:32768
	ds_read_b128 v[192:195], v187 offset:33792
	ds_read_b128 v[196:199], v187 offset:34816
	ds_read_b128 v[200:203], v187 offset:35840
	ds_read_b128 v[204:207], v187 offset:36864
	ds_read_b128 v[208:211], v187 offset:37888
	ds_read_b128 v[212:215], v187 offset:38912
	ds_read_b128 v[216:219], v187 offset:39936
	global_load_lds_dwordx4 v[220:221], off
	v_lshl_add_u64 v[220:221], s[48:49], 0, v[172:173]
	s_mov_b32 m0, s57
	s_nop 0
	global_load_lds_dwordx4 v[220:221], off
	s_waitcnt vmcnt(8)
	s_waitcnt lgkmcnt(0)
	s_barrier
	s_setprio 1
	s_waitcnt lgkmcnt(0)
	v_mfma_f32_16x16x128_f8f6f4 v[158:161], v[2:9], v[188:195], v[158:161]
	v_mfma_f32_16x16x128_f8f6f4 v[154:157], v[10:17], v[188:195], v[154:157]
	v_mfma_f32_16x16x128_f8f6f4 v[150:153], v[2:9], v[196:203], v[150:153]
	v_mfma_f32_16x16x128_f8f6f4 v[146:149], v[10:17], v[196:203], v[146:149]
	v_mfma_f32_16x16x128_f8f6f4 v[142:145], v[2:9], v[204:211], v[142:145]
	v_mfma_f32_16x16x128_f8f6f4 v[134:137], v[10:17], v[204:211], v[134:137]
	v_mfma_f32_16x16x128_f8f6f4 v[118:121], v[2:9], v[212:219], v[118:121]
	v_mfma_f32_16x16x128_f8f6f4 v[110:113], v[10:17], v[212:219], v[110:113]
	s_setprio 0
	s_setprio 1
	v_mfma_f32_16x16x128_f8f6f4 v[138:141], v[18:25], v[188:195], v[138:141]
	v_mfma_f32_16x16x128_f8f6f4 v[130:133], v[26:33], v[188:195], v[130:133]
	v_mfma_f32_16x16x128_f8f6f4 v[126:129], v[18:25], v[196:203], v[126:129]
	v_mfma_f32_16x16x128_f8f6f4 v[122:125], v[26:33], v[196:203], v[122:125]
	v_mfma_f32_16x16x128_f8f6f4 v[114:117], v[18:25], v[204:211], v[114:117]
	v_mfma_f32_16x16x128_f8f6f4 v[106:109], v[26:33], v[204:211], v[106:109]
	v_mfma_f32_16x16x128_f8f6f4 v[102:105], v[18:25], v[212:219], v[102:105]
	v_mfma_f32_16x16x128_f8f6f4 v[98:101], v[26:33], v[212:219], v[98:101]
	s_setprio 0
	s_barrier
	s_add_i32 s41, s41, s56
	v_lshl_add_u64 v[174:175], v[174:175], 0, s[20:21]
	s_mov_b32 m0, s41
	ds_read_b128 v[188:191], v187 offset:49152
	ds_read_b128 v[192:195], v187 offset:50176
	ds_read_b128 v[196:199], v187 offset:51200
	ds_read_b128 v[200:203], v187 offset:52224
	ds_read_b128 v[204:207], v187 offset:53248
	ds_read_b128 v[208:211], v187 offset:54272
	ds_read_b128 v[212:215], v187 offset:55296
	ds_read_b128 v[216:219], v187 offset:56320
	global_load_lds_dwordx4 v[174:175], off
	s_add_i32 m0, s41, 0x2000
	s_add_u32 s46, s46, 0x40080
	v_lshl_add_u64 v[174:175], v[176:177], 0, s[20:21]
	s_addc_u32 s47, s47, 0
	s_add_i32 s41, s50, s56
	global_load_lds_dwordx4 v[174:175], off
	v_lshl_add_u64 v[174:175], s[46:47], 0, v[164:165]
	s_mov_b32 m0, s41
	s_nop 0
	global_load_lds_dwordx4 v[174:175], off
	v_lshl_add_u64 v[174:175], s[46:47], 0, v[162:163]
	s_add_i32 m0, s41, 0x2000
	s_nop 0
	global_load_lds_dwordx4 v[174:175], off
	v_lshl_add_u64 v[174:175], v[178:179], 0, s[20:21]
	s_mov_b32 m0, s60
	s_nop 0
	global_load_lds_dwordx4 v[174:175], off
	v_lshl_add_u64 v[174:175], v[180:181], 0, s[20:21]
	s_mov_b32 m0, s61
	s_nop 0
	global_load_lds_dwordx4 v[174:175], off
	s_waitcnt vmcnt(8)
	s_waitcnt lgkmcnt(0)
	s_barrier
	s_setprio 1
	s_waitcnt lgkmcnt(0)
	v_mfma_f32_16x16x128_f8f6f4 v[94:97], v[2:9], v[188:195], v[94:97]
	v_mfma_f32_16x16x128_f8f6f4 v[90:93], v[10:17], v[188:195], v[90:93]
	v_mfma_f32_16x16x128_f8f6f4 v[78:81], v[2:9], v[196:203], v[78:81]
	v_mfma_f32_16x16x128_f8f6f4 v[66:69], v[10:17], v[196:203], v[66:69]
	v_mfma_f32_16x16x128_f8f6f4 v[50:53], v[2:9], v[204:211], v[50:53]
	v_mfma_f32_16x16x128_f8f6f4 v[46:49], v[10:17], v[204:211], v[46:49]
	v_mfma_f32_16x16x128_f8f6f4 v[38:41], v[2:9], v[212:219], v[38:41]
	v_mfma_f32_16x16x128_f8f6f4 v[34:37], v[10:17], v[212:219], v[34:37]
	s_setprio 0
	s_setprio 1
	v_mfma_f32_16x16x128_f8f6f4 v[82:85], v[18:25], v[188:195], v[82:85]
	v_mfma_f32_16x16x128_f8f6f4 v[70:73], v[26:33], v[188:195], v[70:73]
	v_mfma_f32_16x16x128_f8f6f4 v[54:57], v[18:25], v[196:203], v[54:57]
	v_mfma_f32_16x16x128_f8f6f4 v[42:45], v[26:33], v[196:203], v[42:45]
	v_mfma_f32_16x16x128_f8f6f4 v[74:77], v[18:25], v[204:211], v[74:77]
	v_mfma_f32_16x16x128_f8f6f4 v[86:89], v[26:33], v[204:211], v[86:89]
	v_mfma_f32_16x16x128_f8f6f4 v[58:61], v[18:25], v[212:219], v[58:61]
	v_mfma_f32_16x16x128_f8f6f4 v[62:65], v[26:33], v[212:219], v[62:65]
	s_setprio 0
	s_barrier
	s_add_i32 s37, s37, 2
